# speedup vs baseline: 1.0111x; 1.0111x over previous
.Lg1_loop:
	ds_read_b128 v[152:155], v94
	ds_read_b128 v[136:139], v92
	ds_read_b128 v[156:159], v94 offset:2048
	ds_read_b128 v[140:143], v92 offset:2048
	ds_read_b128 v[160:163], v94 offset:4096
	ds_read_b128 v[144:147], v92 offset:4096
	s_add_i32 s18, s16, 3
	s_lshl_b32 s18, s18, 7
	s_add_u32 s22, s12, s18
	s_addc_u32 s23, s13, 0
	s_add_u32 s24, s14, s18
	s_addc_u32 s25, s15, 0
	s_add_i32 s26, s17, s20
	s_add_i32 s30, s26, s29
	s_add_i32 s27, s17, 0xd000
	s_cmp_lg_u32 s27, 0x27000
	s_cselect_b32 s27, s27, 0
	s_waitcnt lgkmcnt(6)
	v_mfma_f32_16x16x32_f16 v[34:37], v[116:119], v[100:103], v[34:37]
	v_mfma_f32_16x16x32_f16 v[78:81], v[120:123], v[100:103], v[78:81]
	ds_read_b128 v[164:167], v94 offset:6144
	v_mfma_f32_16x16x32_f16 v[74:77], v[124:127], v[100:103], v[74:77]
	ds_read_b128 v[148:151], v92 offset:6144
	v_mfma_f32_16x16x32_f16 v[70:73], v[128:131], v[100:103], v[70:73]
	ds_read_b128 v[168:171], v94 offset:8192
	v_mfma_f32_16x16x32_f16 v[62:65], v[132:135], v[100:103], v[62:65]
	v_mfma_f32_16x16x32_f16 v[58:61], v[116:119], v[104:107], v[58:61]
	v_mfma_f32_16x16x32_f16 v[54:57], v[120:123], v[104:107], v[54:57]
	v_add_u32_e32 v91, s27, v89
	v_mfma_f32_16x16x32_f16 v[50:53], v[124:127], v[104:107], v[50:53]
	v_mfma_f32_16x16x32_f16 v[46:49], v[128:131], v[104:107], v[46:49]
	v_add_u32_e32 v93, s27, v90
	v_mfma_f32_16x16x32_f16 v[42:45], v[132:135], v[104:107], v[42:45]
	v_mfma_f32_16x16x32_f16 v[38:41], v[116:119], v[108:111], v[38:41]
	v_xor_b32_e32 v92, 64, v91
	v_mfma_f32_16x16x32_f16 v[30:33], v[120:123], v[108:111], v[30:33]
	v_mfma_f32_16x16x32_f16 v[26:29], v[124:127], v[108:111], v[26:29]
	v_xor_b32_e32 v94, 64, v93
	v_mfma_f32_16x16x32_f16 v[22:25], v[128:131], v[108:111], v[22:25]
	v_mfma_f32_16x16x32_f16 v[18:21], v[132:135], v[108:111], v[18:21]
	v_mfma_f32_16x16x32_f16 v[14:17], v[116:119], v[112:115], v[14:17]
	v_mfma_f32_16x16x32_f16 v[10:13], v[120:123], v[112:115], v[10:13]
	v_mfma_f32_16x16x32_f16 v[2:5], v[124:127], v[112:115], v[2:5]
	v_mfma_f32_16x16x32_f16 v[6:9], v[128:131], v[112:115], v[6:9]
	v_mfma_f32_16x16x32_f16 v[66:69], v[132:135], v[112:115], v[66:69]
	s_waitcnt vmcnt(7)
	s_waitcnt lgkmcnt(0)
	s_barrier
	ds_read_b128 v[116:119], v93
	ds_read_b128 v[100:103], v91
	ds_read_b128 v[120:123], v93 offset:2048
	ds_read_b128 v[104:107], v91 offset:2048
	ds_read_b128 v[124:127], v93 offset:4096
	ds_read_b128 v[108:111], v91 offset:4096
	ds_read_b128 v[128:131], v93 offset:6144
	ds_read_b128 v[112:115], v91 offset:6144
	ds_read_b128 v[132:135], v93 offset:8192
	v_mfma_f32_16x16x32_f16 v[34:37], v[152:155], v[136:139], v[34:37]
	v_mfma_f32_16x16x32_f16 v[78:81], v[156:159], v[136:139], v[78:81]
	v_mfma_f32_16x16x32_f16 v[74:77], v[160:163], v[136:139], v[74:77]
	s_mov_b32 m0, s26
	s_add_i32 s26, s26, 0x2000
	global_load_lds_dwordx4 v82, s[22:23]
	v_mfma_f32_16x16x32_f16 v[70:73], v[164:167], v[136:139], v[70:73]
	v_mfma_f32_16x16x32_f16 v[62:65], v[168:171], v[136:139], v[62:65]
	v_mfma_f32_16x16x32_f16 v[58:61], v[152:155], v[140:143], v[58:61]
	s_mov_b32 m0, s26
	s_add_i32 s26, s26, 0x2000
	global_load_lds_dwordx4 v83, s[22:23]
	v_mfma_f32_16x16x32_f16 v[54:57], v[156:159], v[140:143], v[54:57]
	v_mfma_f32_16x16x32_f16 v[50:53], v[160:163], v[140:143], v[50:53]
	v_mfma_f32_16x16x32_f16 v[46:49], v[164:167], v[140:143], v[46:49]
	s_mov_b32 m0, s26
	s_add_i32 s26, s26, 0x2000
	global_load_lds_dwordx4 v84, s[22:23]
	v_mfma_f32_16x16x32_f16 v[42:45], v[168:171], v[140:143], v[42:45]
	v_mfma_f32_16x16x32_f16 v[38:41], v[152:155], v[144:147], v[38:41]
	v_mfma_f32_16x16x32_f16 v[30:33], v[156:159], v[144:147], v[30:33]
	s_mov_b32 m0, s26
	s_add_i32 s26, s26, 0x2000
	global_load_lds_dwordx4 v85, s[22:23]
	v_mfma_f32_16x16x32_f16 v[26:29], v[160:163], v[144:147], v[26:29]
	v_mfma_f32_16x16x32_f16 v[22:25], v[164:167], v[144:147], v[22:25]
	v_mfma_f32_16x16x32_f16 v[18:21], v[168:171], v[144:147], v[18:21]
	s_mov_b32 m0, s26
	s_add_i32 s26, s26, 0x2000
	global_load_lds_dwordx4 v86, s[24:25]
	v_mfma_f32_16x16x32_f16 v[14:17], v[152:155], v[148:151], v[14:17]
	v_mfma_f32_16x16x32_f16 v[10:13], v[156:159], v[148:151], v[10:13]
	v_mfma_f32_16x16x32_f16 v[2:5], v[160:163], v[148:151], v[2:5]
	s_mov_b32 m0, s26
	s_add_i32 s26, s26, 0x2000
	global_load_lds_dwordx4 v87, s[24:25]
	v_mfma_f32_16x16x32_f16 v[6:9], v[164:167], v[148:151], v[6:9]
	v_mfma_f32_16x16x32_f16 v[66:69], v[168:171], v[148:151], v[66:69]
	s_mov_b32 m0, s30
	s_nop 0
	global_load_lds_dwordx4 v88, s[24:25]
	s_mov_b32 s17, s27
	s_add_i32 s16, s16, 1
	s_cmp_lt_u32 s16, 13
	s_cbranch_scc1 .Lg1_loop
	ds_read_b128 v[152:155], v94
	ds_read_b128 v[136:139], v92
	ds_read_b128 v[156:159], v94 offset:2048
	ds_read_b128 v[140:143], v92 offset:2048
	ds_read_b128 v[160:163], v94 offset:4096
	ds_read_b128 v[144:147], v92 offset:4096
	s_add_i32 s27, s17, 0xd000
	s_cmp_lg_u32 s27, 0x27000
	s_cselect_b32 s27, s27, 0
	s_waitcnt lgkmcnt(6)
	v_mfma_f32_16x16x32_f16 v[34:37], v[116:119], v[100:103], v[34:37]
	v_mfma_f32_16x16x32_f16 v[78:81], v[120:123], v[100:103], v[78:81]
	ds_read_b128 v[164:167], v94 offset:6144
	v_mfma_f32_16x16x32_f16 v[74:77], v[124:127], v[100:103], v[74:77]
	ds_read_b128 v[148:151], v92 offset:6144
	v_mfma_f32_16x16x32_f16 v[70:73], v[128:131], v[100:103], v[70:73]
	ds_read_b128 v[168:171], v94 offset:8192
	v_mfma_f32_16x16x32_f16 v[62:65], v[132:135], v[100:103], v[62:65]
	v_mfma_f32_16x16x32_f16 v[58:61], v[116:119], v[104:107], v[58:61]
	v_mfma_f32_16x16x32_f16 v[54:57], v[120:123], v[104:107], v[54:57]
	v_add_u32_e32 v91, s27, v89
	v_mfma_f32_16x16x32_f16 v[50:53], v[124:127], v[104:107], v[50:53]
	v_mfma_f32_16x16x32_f16 v[46:49], v[128:131], v[104:107], v[46:49]
	v_add_u32_e32 v93, s27, v90
	v_mfma_f32_16x16x32_f16 v[42:45], v[132:135], v[104:107], v[42:45]
	v_mfma_f32_16x16x32_f16 v[38:41], v[116:119], v[108:111], v[38:41]
	v_xor_b32_e32 v92, 64, v91
	v_mfma_f32_16x16x32_f16 v[30:33], v[120:123], v[108:111], v[30:33]
	v_mfma_f32_16x16x32_f16 v[26:29], v[124:127], v[108:111], v[26:29]
	v_xor_b32_e32 v94, 64, v93
	v_mfma_f32_16x16x32_f16 v[22:25], v[128:131], v[108:111], v[22:25]
	v_mfma_f32_16x16x32_f16 v[18:21], v[132:135], v[108:111], v[18:21]
	v_mfma_f32_16x16x32_f16 v[14:17], v[116:119], v[112:115], v[14:17]
	v_mfma_f32_16x16x32_f16 v[10:13], v[120:123], v[112:115], v[10:13]
	v_mfma_f32_16x16x32_f16 v[2:5], v[124:127], v[112:115], v[2:5]
	v_mfma_f32_16x16x32_f16 v[6:9], v[128:131], v[112:115], v[6:9]
	v_mfma_f32_16x16x32_f16 v[66:69], v[132:135], v[112:115], v[66:69]
	s_waitcnt vmcnt(7)
	s_waitcnt lgkmcnt(0)
	s_barrier
	ds_read_b128 v[116:119], v93
	ds_read_b128 v[100:103], v91
	ds_read_b128 v[120:123], v93 offset:2048
	ds_read_b128 v[104:107], v91 offset:2048
	ds_read_b128 v[124:127], v93 offset:4096
	ds_read_b128 v[108:111], v91 offset:4096
	ds_read_b128 v[128:131], v93 offset:6144
	ds_read_b128 v[112:115], v91 offset:6144
	ds_read_b128 v[132:135], v93 offset:8192
	v_mfma_f32_16x16x32_f16 v[34:37], v[152:155], v[136:139], v[34:37]
	v_mfma_f32_16x16x32_f16 v[78:81], v[156:159], v[136:139], v[78:81]
	v_mfma_f32_16x16x32_f16 v[74:77], v[160:163], v[136:139], v[74:77]
	v_mfma_f32_16x16x32_f16 v[70:73], v[164:167], v[136:139], v[70:73]
	v_mfma_f32_16x16x32_f16 v[62:65], v[168:171], v[136:139], v[62:65]
	v_mfma_f32_16x16x32_f16 v[58:61], v[152:155], v[140:143], v[58:61]
	v_mfma_f32_16x16x32_f16 v[54:57], v[156:159], v[140:143], v[54:57]
	v_mfma_f32_16x16x32_f16 v[50:53], v[160:163], v[140:143], v[50:53]
	v_mfma_f32_16x16x32_f16 v[46:49], v[164:167], v[140:143], v[46:49]
	v_mfma_f32_16x16x32_f16 v[42:45], v[168:171], v[140:143], v[42:45]
	v_mfma_f32_16x16x32_f16 v[38:41], v[152:155], v[144:147], v[38:41]
	v_mfma_f32_16x16x32_f16 v[30:33], v[156:159], v[144:147], v[30:33]
	v_mfma_f32_16x16x32_f16 v[26:29], v[160:163], v[144:147], v[26:29]
	v_mfma_f32_16x16x32_f16 v[22:25], v[164:167], v[144:147], v[22:25]
	v_mfma_f32_16x16x32_f16 v[18:21], v[168:171], v[144:147], v[18:21]
	v_mfma_f32_16x16x32_f16 v[14:17], v[152:155], v[148:151], v[14:17]
	v_mfma_f32_16x16x32_f16 v[10:13], v[156:159], v[148:151], v[10:13]
	v_mfma_f32_16x16x32_f16 v[2:5], v[160:163], v[148:151], v[2:5]
	v_mfma_f32_16x16x32_f16 v[6:9], v[164:167], v[148:151], v[6:9]
	v_mfma_f32_16x16x32_f16 v[66:69], v[168:171], v[148:151], v[66:69]
	s_mov_b32 s17, s27
	ds_read_b128 v[152:155], v94
	ds_read_b128 v[136:139], v92
	ds_read_b128 v[156:159], v94 offset:2048
	ds_read_b128 v[140:143], v92 offset:2048
	ds_read_b128 v[160:163], v94 offset:4096
	ds_read_b128 v[144:147], v92 offset:4096
	s_add_i32 s27, s17, 0xd000
	s_cmp_lg_u32 s27, 0x27000
	s_cselect_b32 s27, s27, 0
	s_waitcnt lgkmcnt(6)
	v_mfma_f32_16x16x32_f16 v[34:37], v[116:119], v[100:103], v[34:37]
	v_mfma_f32_16x16x32_f16 v[78:81], v[120:123], v[100:103], v[78:81]
	ds_read_b128 v[164:167], v94 offset:6144
	v_mfma_f32_16x16x32_f16 v[74:77], v[124:127], v[100:103], v[74:77]
	ds_read_b128 v[148:151], v92 offset:6144
	v_mfma_f32_16x16x32_f16 v[70:73], v[128:131], v[100:103], v[70:73]
	ds_read_b128 v[168:171], v94 offset:8192
	v_mfma_f32_16x16x32_f16 v[62:65], v[132:135], v[100:103], v[62:65]
	v_mfma_f32_16x16x32_f16 v[58:61], v[116:119], v[104:107], v[58:61]
	v_mfma_f32_16x16x32_f16 v[54:57], v[120:123], v[104:107], v[54:57]
	v_add_u32_e32 v91, s27, v89
	v_mfma_f32_16x16x32_f16 v[50:53], v[124:127], v[104:107], v[50:53]
	v_mfma_f32_16x16x32_f16 v[46:49], v[128:131], v[104:107], v[46:49]
	v_add_u32_e32 v93, s27, v90
	v_mfma_f32_16x16x32_f16 v[42:45], v[132:135], v[104:107], v[42:45]
	v_mfma_f32_16x16x32_f16 v[38:41], v[116:119], v[108:111], v[38:41]
	v_xor_b32_e32 v92, 64, v91
	v_mfma_f32_16x16x32_f16 v[30:33], v[120:123], v[108:111], v[30:33]
	v_mfma_f32_16x16x32_f16 v[26:29], v[124:127], v[108:111], v[26:29]
	v_xor_b32_e32 v94, 64, v93
	v_mfma_f32_16x16x32_f16 v[22:25], v[128:131], v[108:111], v[22:25]
	v_mfma_f32_16x16x32_f16 v[18:21], v[132:135], v[108:111], v[18:21]
	v_mfma_f32_16x16x32_f16 v[14:17], v[116:119], v[112:115], v[14:17]
	v_mfma_f32_16x16x32_f16 v[10:13], v[120:123], v[112:115], v[10:13]
	v_mfma_f32_16x16x32_f16 v[2:5], v[124:127], v[112:115], v[2:5]
	v_mfma_f32_16x16x32_f16 v[6:9], v[128:131], v[112:115], v[6:9]
	v_mfma_f32_16x16x32_f16 v[66:69], v[132:135], v[112:115], v[66:69]
	s_waitcnt vmcnt(0)
	s_waitcnt lgkmcnt(0)
	s_barrier
	ds_read_b128 v[116:119], v93
	ds_read_b128 v[100:103], v91
	ds_read_b128 v[120:123], v93 offset:2048
	ds_read_b128 v[104:107], v91 offset:2048
	ds_read_b128 v[124:127], v93 offset:4096
	ds_read_b128 v[108:111], v91 offset:4096
	ds_read_b128 v[128:131], v93 offset:6144
	ds_read_b128 v[112:115], v91 offset:6144
	ds_read_b128 v[132:135], v93 offset:8192
	v_mfma_f32_16x16x32_f16 v[34:37], v[152:155], v[136:139], v[34:37]
	v_mfma_f32_16x16x32_f16 v[78:81], v[156:159], v[136:139], v[78:81]
	v_mfma_f32_16x16x32_f16 v[74:77], v[160:163], v[136:139], v[74:77]
	v_mfma_f32_16x16x32_f16 v[70:73], v[164:167], v[136:139], v[70:73]
	v_mfma_f32_16x16x32_f16 v[62:65], v[168:171], v[136:139], v[62:65]
	v_mfma_f32_16x16x32_f16 v[58:61], v[152:155], v[140:143], v[58:61]
	v_mfma_f32_16x16x32_f16 v[54:57], v[156:159], v[140:143], v[54:57]
	v_mfma_f32_16x16x32_f16 v[50:53], v[160:163], v[140:143], v[50:53]
	v_mfma_f32_16x16x32_f16 v[46:49], v[164:167], v[140:143], v[46:49]
	v_mfma_f32_16x16x32_f16 v[42:45], v[168:171], v[140:143], v[42:45]
	v_mfma_f32_16x16x32_f16 v[38:41], v[152:155], v[144:147], v[38:41]
	v_mfma_f32_16x16x32_f16 v[30:33], v[156:159], v[144:147], v[30:33]
	v_mfma_f32_16x16x32_f16 v[26:29], v[160:163], v[144:147], v[26:29]
	v_mfma_f32_16x16x32_f16 v[22:25], v[164:167], v[144:147], v[22:25]
	v_mfma_f32_16x16x32_f16 v[18:21], v[168:171], v[144:147], v[18:21]
	v_mfma_f32_16x16x32_f16 v[14:17], v[152:155], v[148:151], v[14:17]
	v_mfma_f32_16x16x32_f16 v[10:13], v[156:159], v[148:151], v[10:13]
	v_mfma_f32_16x16x32_f16 v[2:5], v[160:163], v[148:151], v[2:5]
	v_mfma_f32_16x16x32_f16 v[6:9], v[164:167], v[148:151], v[6:9]
	v_mfma_f32_16x16x32_f16 v[66:69], v[168:171], v[148:151], v[66:69]
	s_mov_b32 s17, s27
	ds_read_b128 v[152:155], v94
	ds_read_b128 v[136:139], v92
	ds_read_b128 v[156:159], v94 offset:2048
	ds_read_b128 v[140:143], v92 offset:2048
	ds_read_b128 v[160:163], v94 offset:4096
	ds_read_b128 v[144:147], v92 offset:4096
	s_add_i32 s27, s17, 0xd000
	s_cmp_lg_u32 s27, 0x27000
	s_cselect_b32 s27, s27, 0
	s_waitcnt lgkmcnt(6)
	v_mfma_f32_16x16x32_f16 v[34:37], v[116:119], v[100:103], v[34:37]
	v_mfma_f32_16x16x32_f16 v[78:81], v[120:123], v[100:103], v[78:81]
	ds_read_b128 v[164:167], v94 offset:6144
	v_mfma_f32_16x16x32_f16 v[74:77], v[124:127], v[100:103], v[74:77]
	ds_read_b128 v[148:151], v92 offset:6144
	v_mfma_f32_16x16x32_f16 v[70:73], v[128:131], v[100:103], v[70:73]
	ds_read_b128 v[168:171], v94 offset:8192
	v_mfma_f32_16x16x32_f16 v[62:65], v[132:135], v[100:103], v[62:65]
	v_mfma_f32_16x16x32_f16 v[58:61], v[116:119], v[104:107], v[58:61]
	v_mfma_f32_16x16x32_f16 v[54:57], v[120:123], v[104:107], v[54:57]
	v_add_u32_e32 v91, s27, v89
	v_mfma_f32_16x16x32_f16 v[50:53], v[124:127], v[104:107], v[50:53]
	v_mfma_f32_16x16x32_f16 v[46:49], v[128:131], v[104:107], v[46:49]
	v_add_u32_e32 v93, s27, v90
	v_mfma_f32_16x16x32_f16 v[42:45], v[132:135], v[104:107], v[42:45]
	v_mfma_f32_16x16x32_f16 v[38:41], v[116:119], v[108:111], v[38:41]
	v_xor_b32_e32 v92, 64, v91
	v_mfma_f32_16x16x32_f16 v[30:33], v[120:123], v[108:111], v[30:33]
	v_mfma_f32_16x16x32_f16 v[26:29], v[124:127], v[108:111], v[26:29]
	v_xor_b32_e32 v94, 64, v93
	v_mfma_f32_16x16x32_f16 v[22:25], v[128:131], v[108:111], v[22:25]
	v_mfma_f32_16x16x32_f16 v[18:21], v[132:135], v[108:111], v[18:21]
	v_mfma_f32_16x16x32_f16 v[14:17], v[116:119], v[112:115], v[14:17]
	v_mfma_f32_16x16x32_f16 v[10:13], v[120:123], v[112:115], v[10:13]
	v_mfma_f32_16x16x32_f16 v[2:5], v[124:127], v[112:115], v[2:5]
	v_mfma_f32_16x16x32_f16 v[6:9], v[128:131], v[112:115], v[6:9]
	v_mfma_f32_16x16x32_f16 v[66:69], v[132:135], v[112:115], v[66:69]
	s_waitcnt lgkmcnt(0)
	s_barrier
	ds_read_b128 v[116:119], v93
	ds_read_b128 v[100:103], v91
	ds_read_b128 v[120:123], v93 offset:2048
	ds_read_b128 v[104:107], v91 offset:2048
	ds_read_b128 v[124:127], v93 offset:4096
	ds_read_b128 v[108:111], v91 offset:4096
	ds_read_b128 v[128:131], v93 offset:6144
	ds_read_b128 v[112:115], v91 offset:6144
	ds_read_b128 v[132:135], v93 offset:8192
	v_mfma_f32_16x16x32_f16 v[34:37], v[152:155], v[136:139], v[34:37]
	v_mfma_f32_16x16x32_f16 v[78:81], v[156:159], v[136:139], v[78:81]
	v_mfma_f32_16x16x32_f16 v[74:77], v[160:163], v[136:139], v[74:77]
	v_mfma_f32_16x16x32_f16 v[70:73], v[164:167], v[136:139], v[70:73]
	v_mfma_f32_16x16x32_f16 v[62:65], v[168:171], v[136:139], v[62:65]
	v_mfma_f32_16x16x32_f16 v[58:61], v[152:155], v[140:143], v[58:61]
	v_mfma_f32_16x16x32_f16 v[54:57], v[156:159], v[140:143], v[54:57]
	v_mfma_f32_16x16x32_f16 v[50:53], v[160:163], v[140:143], v[50:53]
	v_mfma_f32_16x16x32_f16 v[46:49], v[164:167], v[140:143], v[46:49]
	v_mfma_f32_16x16x32_f16 v[42:45], v[168:171], v[140:143], v[42:45]
	v_mfma_f32_16x16x32_f16 v[38:41], v[152:155], v[144:147], v[38:41]
	v_mfma_f32_16x16x32_f16 v[30:33], v[156:159], v[144:147], v[30:33]
	v_mfma_f32_16x16x32_f16 v[26:29], v[160:163], v[144:147], v[26:29]
	v_mfma_f32_16x16x32_f16 v[22:25], v[164:167], v[144:147], v[22:25]
	v_mfma_f32_16x16x32_f16 v[18:21], v[168:171], v[144:147], v[18:21]
	v_mfma_f32_16x16x32_f16 v[14:17], v[152:155], v[148:151], v[14:17]
	v_mfma_f32_16x16x32_f16 v[10:13], v[156:159], v[148:151], v[10:13]
	v_mfma_f32_16x16x32_f16 v[2:5], v[160:163], v[148:151], v[2:5]
	v_mfma_f32_16x16x32_f16 v[6:9], v[164:167], v[148:151], v[6:9]
	v_mfma_f32_16x16x32_f16 v[66:69], v[168:171], v[148:151], v[66:69]
	s_mov_b32 s17, s27
	s_nop 7

.Lg2_loop:
	ds_read_b128 v[40:43], v12
	ds_read_b128 v[48:51], v10
	ds_read_b128 v[44:47], v12 offset:2048
	ds_read_b128 v[52:55], v10 offset:2048
	ds_read_b128 v[56:59], v10 offset:4096
	ds_read_b128 v[60:63], v10 offset:6144
	s_add_i32 s22, s12, 4
	s_lshl_b32 s22, s22, 7
	s_add_u32 s14, s4, s22
	s_addc_u32 s15, s5, 0
	s_add_u32 s16, s6, s22
	s_addc_u32 s17, s7, 0
	s_add_i32 s21, s13, s20
	s_add_i32 s23, s13, 0x6000
	s_cmp_lg_u32 s23, 0x18000
	s_cselect_b32 s23, s23, 0
	s_waitcnt lgkmcnt(6)
	v_mfma_f32_16x16x32_f16 a[0:3], v[16:19], v[24:27], a[0:3]
	v_mfma_f32_16x16x32_f16 a[4:7], v[20:23], v[24:27], a[4:7]
	v_add_u32_e32 v9, s23, v1
	v_mfma_f32_16x16x32_f16 a[8:11], v[16:19], v[28:31], a[8:11]
	v_mfma_f32_16x16x32_f16 a[12:15], v[20:23], v[28:31], a[12:15]
	v_add_u32_e32 v11, s23, v2
	v_mfma_f32_16x16x32_f16 a[16:19], v[16:19], v[32:35], a[16:19]
	v_mfma_f32_16x16x32_f16 a[20:23], v[20:23], v[32:35], a[20:23]
	v_xor_b32_e32 v10, 64, v9
	v_mfma_f32_16x16x32_f16 a[24:27], v[16:19], v[36:39], a[24:27]
	v_mfma_f32_16x16x32_f16 a[28:31], v[20:23], v[36:39], a[28:31]
	v_xor_b32_e32 v12, 64, v11
	s_waitcnt vmcnt(12)
	s_waitcnt lgkmcnt(0)
	s_barrier
	s_mov_b32 m0, s21
	s_add_i32 s21, s21, 0x1000
	global_load_lds_dwordx4 v3, s[14:15]
	s_mov_b32 m0, s21
	s_add_i32 s21, s21, 0x1000
	global_load_lds_dwordx4 v4, s[14:15]
	s_mov_b32 m0, s21
	s_add_i32 s21, s21, 0x1000
	global_load_lds_dwordx4 v5, s[14:15]
	s_mov_b32 m0, s21
	s_add_i32 s21, s21, 0x1000
	global_load_lds_dwordx4 v6, s[14:15]
	s_mov_b32 m0, s21
	s_add_i32 s21, s21, 0x1000
	global_load_lds_dwordx4 v7, s[16:17]
	s_mov_b32 m0, s21
	s_add_i32 s21, s21, 0x1000
	global_load_lds_dwordx4 v8, s[16:17]
	ds_read_b128 v[16:19], v11
	ds_read_b128 v[24:27], v9
	ds_read_b128 v[20:23], v11 offset:2048
	ds_read_b128 v[28:31], v9 offset:2048
	ds_read_b128 v[32:35], v9 offset:4096
	ds_read_b128 v[36:39], v9 offset:6144
	v_mfma_f32_16x16x32_f16 a[0:3], v[40:43], v[48:51], a[0:3]
	v_mfma_f32_16x16x32_f16 a[4:7], v[44:47], v[48:51], a[4:7]
	v_mfma_f32_16x16x32_f16 a[8:11], v[40:43], v[52:55], a[8:11]
	v_mfma_f32_16x16x32_f16 a[12:15], v[44:47], v[52:55], a[12:15]
	v_mfma_f32_16x16x32_f16 a[16:19], v[40:43], v[56:59], a[16:19]
	v_mfma_f32_16x16x32_f16 a[20:23], v[44:47], v[56:59], a[20:23]
	v_mfma_f32_16x16x32_f16 a[24:27], v[40:43], v[60:63], a[24:27]
	v_mfma_f32_16x16x32_f16 a[28:31], v[44:47], v[60:63], a[28:31]
	s_mov_b32 s13, s23
	s_add_i32 s12, s12, 1
	s_cmp_lt_u32 s12, 20
	s_cbranch_scc1 .Lg2_loop
	ds_read_b128 v[40:43], v12
	ds_read_b128 v[48:51], v10
	ds_read_b128 v[44:47], v12 offset:2048
	ds_read_b128 v[52:55], v10 offset:2048
	ds_read_b128 v[56:59], v10 offset:4096
	ds_read_b128 v[60:63], v10 offset:6144
	s_add_i32 s23, s13, 0x6000
	s_cmp_lg_u32 s23, 0x18000
	s_cselect_b32 s23, s23, 0
	s_waitcnt lgkmcnt(6)
	v_mfma_f32_16x16x32_f16 a[0:3], v[16:19], v[24:27], a[0:3]
	v_mfma_f32_16x16x32_f16 a[4:7], v[20:23], v[24:27], a[4:7]
	v_add_u32_e32 v9, s23, v1
	v_mfma_f32_16x16x32_f16 a[8:11], v[16:19], v[28:31], a[8:11]
	v_mfma_f32_16x16x32_f16 a[12:15], v[20:23], v[28:31], a[12:15]
	v_add_u32_e32 v11, s23, v2
	v_mfma_f32_16x16x32_f16 a[16:19], v[16:19], v[32:35], a[16:19]
	v_mfma_f32_16x16x32_f16 a[20:23], v[20:23], v[32:35], a[20:23]
	v_xor_b32_e32 v10, 64, v9
	v_mfma_f32_16x16x32_f16 a[24:27], v[16:19], v[36:39], a[24:27]
	v_mfma_f32_16x16x32_f16 a[28:31], v[20:23], v[36:39], a[28:31]
	v_xor_b32_e32 v12, 64, v11
	s_waitcnt vmcnt(12)
	s_waitcnt lgkmcnt(0)
	s_barrier
	ds_read_b128 v[16:19], v11
	ds_read_b128 v[24:27], v9
	ds_read_b128 v[20:23], v11 offset:2048
	ds_read_b128 v[28:31], v9 offset:2048
	ds_read_b128 v[32:35], v9 offset:4096
	ds_read_b128 v[36:39], v9 offset:6144
	v_mfma_f32_16x16x32_f16 a[0:3], v[40:43], v[48:51], a[0:3]
	v_mfma_f32_16x16x32_f16 a[4:7], v[44:47], v[48:51], a[4:7]
	v_mfma_f32_16x16x32_f16 a[8:11], v[40:43], v[52:55], a[8:11]
	v_mfma_f32_16x16x32_f16 a[12:15], v[44:47], v[52:55], a[12:15]
	v_mfma_f32_16x16x32_f16 a[16:19], v[40:43], v[56:59], a[16:19]
	v_mfma_f32_16x16x32_f16 a[20:23], v[44:47], v[56:59], a[20:23]
	v_mfma_f32_16x16x32_f16 a[24:27], v[40:43], v[60:63], a[24:27]
	v_mfma_f32_16x16x32_f16 a[28:31], v[44:47], v[60:63], a[28:31]
	s_mov_b32 s13, s23
	ds_read_b128 v[40:43], v12
	ds_read_b128 v[48:51], v10
	ds_read_b128 v[44:47], v12 offset:2048
	ds_read_b128 v[52:55], v10 offset:2048
	ds_read_b128 v[56:59], v10 offset:4096
	ds_read_b128 v[60:63], v10 offset:6144
	s_add_i32 s23, s13, 0x6000
	s_cmp_lg_u32 s23, 0x18000
	s_cselect_b32 s23, s23, 0
	s_waitcnt lgkmcnt(6)
	v_mfma_f32_16x16x32_f16 a[0:3], v[16:19], v[24:27], a[0:3]
	v_mfma_f32_16x16x32_f16 a[4:7], v[20:23], v[24:27], a[4:7]
	v_add_u32_e32 v9, s23, v1
	v_mfma_f32_16x16x32_f16 a[8:11], v[16:19], v[28:31], a[8:11]
	v_mfma_f32_16x16x32_f16 a[12:15], v[20:23], v[28:31], a[12:15]
	v_add_u32_e32 v11, s23, v2
	v_mfma_f32_16x16x32_f16 a[16:19], v[16:19], v[32:35], a[16:19]
	v_mfma_f32_16x16x32_f16 a[20:23], v[20:23], v[32:35], a[20:23]
	v_xor_b32_e32 v10, 64, v9
	v_mfma_f32_16x16x32_f16 a[24:27], v[16:19], v[36:39], a[24:27]
	v_mfma_f32_16x16x32_f16 a[28:31], v[20:23], v[36:39], a[28:31]
	v_xor_b32_e32 v12, 64, v11
	s_waitcnt vmcnt(6)
	s_waitcnt lgkmcnt(0)
	s_barrier
	ds_read_b128 v[16:19], v11
	ds_read_b128 v[24:27], v9
	ds_read_b128 v[20:23], v11 offset:2048
	ds_read_b128 v[28:31], v9 offset:2048
	ds_read_b128 v[32:35], v9 offset:4096
	ds_read_b128 v[36:39], v9 offset:6144
	v_mfma_f32_16x16x32_f16 a[0:3], v[40:43], v[48:51], a[0:3]
	v_mfma_f32_16x16x32_f16 a[4:7], v[44:47], v[48:51], a[4:7]
	v_mfma_f32_16x16x32_f16 a[8:11], v[40:43], v[52:55], a[8:11]
	v_mfma_f32_16x16x32_f16 a[12:15], v[44:47], v[52:55], a[12:15]
	v_mfma_f32_16x16x32_f16 a[16:19], v[40:43], v[56:59], a[16:19]
	v_mfma_f32_16x16x32_f16 a[20:23], v[44:47], v[56:59], a[20:23]
	v_mfma_f32_16x16x32_f16 a[24:27], v[40:43], v[60:63], a[24:27]
	v_mfma_f32_16x16x32_f16 a[28:31], v[44:47], v[60:63], a[28:31]
	s_mov_b32 s13, s23
	ds_read_b128 v[40:43], v12
	ds_read_b128 v[48:51], v10
	ds_read_b128 v[44:47], v12 offset:2048
	ds_read_b128 v[52:55], v10 offset:2048
	ds_read_b128 v[56:59], v10 offset:4096
	ds_read_b128 v[60:63], v10 offset:6144
	s_add_i32 s23, s13, 0x6000
	s_cmp_lg_u32 s23, 0x18000
	s_cselect_b32 s23, s23, 0
	s_waitcnt lgkmcnt(6)
	v_mfma_f32_16x16x32_f16 a[0:3], v[16:19], v[24:27], a[0:3]
	v_mfma_f32_16x16x32_f16 a[4:7], v[20:23], v[24:27], a[4:7]
	v_add_u32_e32 v9, s23, v1
	v_mfma_f32_16x16x32_f16 a[8:11], v[16:19], v[28:31], a[8:11]
	v_mfma_f32_16x16x32_f16 a[12:15], v[20:23], v[28:31], a[12:15]
	v_add_u32_e32 v11, s23, v2
	v_mfma_f32_16x16x32_f16 a[16:19], v[16:19], v[32:35], a[16:19]
	v_mfma_f32_16x16x32_f16 a[20:23], v[20:23], v[32:35], a[20:23]
	v_xor_b32_e32 v10, 64, v9
	v_mfma_f32_16x16x32_f16 a[24:27], v[16:19], v[36:39], a[24:27]
	v_mfma_f32_16x16x32_f16 a[28:31], v[20:23], v[36:39], a[28:31]
	v_xor_b32_e32 v12, 64, v11
	s_waitcnt vmcnt(0)
	s_waitcnt lgkmcnt(0)
	s_barrier
	ds_read_b128 v[16:19], v11
	ds_read_b128 v[24:27], v9
	ds_read_b128 v[20:23], v11 offset:2048
	ds_read_b128 v[28:31], v9 offset:2048
	ds_read_b128 v[32:35], v9 offset:4096
	ds_read_b128 v[36:39], v9 offset:6144
	v_mfma_f32_16x16x32_f16 a[0:3], v[40:43], v[48:51], a[0:3]
	v_mfma_f32_16x16x32_f16 a[4:7], v[44:47], v[48:51], a[4:7]
	v_mfma_f32_16x16x32_f16 a[8:11], v[40:43], v[52:55], a[8:11]
	v_mfma_f32_16x16x32_f16 a[12:15], v[44:47], v[52:55], a[12:15]
	v_mfma_f32_16x16x32_f16 a[16:19], v[40:43], v[56:59], a[16:19]
	v_mfma_f32_16x16x32_f16 a[20:23], v[44:47], v[56:59], a[20:23]
	v_mfma_f32_16x16x32_f16 a[24:27], v[40:43], v[60:63], a[24:27]
	v_mfma_f32_16x16x32_f16 a[28:31], v[44:47], v[60:63], a[28:31]
	s_mov_b32 s13, s23
	ds_read_b128 v[40:43], v12
	ds_read_b128 v[48:51], v10
	ds_read_b128 v[44:47], v12 offset:2048
	ds_read_b128 v[52:55], v10 offset:2048
	ds_read_b128 v[56:59], v10 offset:4096
	ds_read_b128 v[60:63], v10 offset:6144
	s_add_i32 s23, s13, 0x6000
	s_cmp_lg_u32 s23, 0x18000
	s_cselect_b32 s23, s23, 0
	s_waitcnt lgkmcnt(6)
	v_mfma_f32_16x16x32_f16 a[0:3], v[16:19], v[24:27], a[0:3]
	v_mfma_f32_16x16x32_f16 a[4:7], v[20:23], v[24:27], a[4:7]
	v_add_u32_e32 v9, s23, v1
	v_mfma_f32_16x16x32_f16 a[8:11], v[16:19], v[28:31], a[8:11]
	v_mfma_f32_16x16x32_f16 a[12:15], v[20:23], v[28:31], a[12:15]
	v_add_u32_e32 v11, s23, v2
	v_mfma_f32_16x16x32_f16 a[16:19], v[16:19], v[32:35], a[16:19]
	v_mfma_f32_16x16x32_f16 a[20:23], v[20:23], v[32:35], a[20:23]
	v_xor_b32_e32 v10, 64, v9
	v_mfma_f32_16x16x32_f16 a[24:27], v[16:19], v[36:39], a[24:27]
	v_mfma_f32_16x16x32_f16 a[28:31], v[20:23], v[36:39], a[28:31]
	v_xor_b32_e32 v12, 64, v11
	s_waitcnt lgkmcnt(0)
	s_barrier
	ds_read_b128 v[16:19], v11
	ds_read_b128 v[24:27], v9
	ds_read_b128 v[20:23], v11 offset:2048
	ds_read_b128 v[28:31], v9 offset:2048
	ds_read_b128 v[32:35], v9 offset:4096
	ds_read_b128 v[36:39], v9 offset:6144
	v_mfma_f32_16x16x32_f16 a[0:3], v[40:43], v[48:51], a[0:3]
	v_mfma_f32_16x16x32_f16 a[4:7], v[44:47], v[48:51], a[4:7]
	v_mfma_f32_16x16x32_f16 a[8:11], v[40:43], v[52:55], a[8:11]
	v_mfma_f32_16x16x32_f16 a[12:15], v[44:47], v[52:55], a[12:15]
	v_mfma_f32_16x16x32_f16 a[16:19], v[40:43], v[56:59], a[16:19]
	v_mfma_f32_16x16x32_f16 a[20:23], v[44:47], v[56:59], a[20:23]
	v_mfma_f32_16x16x32_f16 a[24:27], v[40:43], v[60:63], a[24:27]
	v_mfma_f32_16x16x32_f16 a[28:31], v[44:47], v[60:63], a[28:31]
	s_mov_b32 s13, s23
	s_waitcnt vmcnt(0) lgkmcnt(0)
	v_and_b32_e32 v13, 15, v0
	v_lshrrev_b32_e32 v14, 7, v0
	v_lshl_add_u32 v13, v14, 6, v13
	v_add_u32_e32 v13, s10, v13
	v_bfe_u32 v14, v0, 6, 1
	v_bfe_u32 v15, v0, 4, 2
	v_lshlrev_b32_e32 v14, 5, v14
	v_lshl_add_u32 v14, v15, 2, v14
	v_add_u32_e32 v14, s11, v14
	v_lshlrev_b32_e32 v13, 10, v13
	v_add_u32_e32 v13, v13, v14
	v_lshlrev_b32_e32 v13, 2, v13
	v_add_u32_e32 v14, 0x10000, v13
	v_add_u32_e32 v15, 0x20000, v13
	v_add_u32_e32 v16, 0x30000, v13
	s_nop 7
	global_store_dwordx4 v13, a[0:3], s[8:9]
	global_store_dwordx4 v13, a[4:7], s[8:9] offset:64
	global_store_dwordx4 v14, a[8:11], s[8:9]
	global_store_dwordx4 v14, a[12:15], s[8:9] offset:64
	global_store_dwordx4 v15, a[16:19], s[8:9]
	global_store_dwordx4 v15, a[20:23], s[8:9] offset:64
	global_store_dwordx4 v16, a[24:27], s[8:9]
	global_store_dwordx4 v16, a[28:31], s[8:9] offset:64
	s_endpgm
	.p2alignl 8, 3212836864
